# weight-conversion queue moved from phase 1 (beside the layer-0 GEMM) to phase 4: odd-XCD workgroups convert then join the attention queues; layer-0 GEMM on all 256 workgroups; conversion loop unrolled
# speedup vs baseline: 1.0471x; 1.0418x over previous
_Z10fwd_kernel6Params:
	s_mov_b32 s100, 0
	s_load_dwordx4 s[88:91], s[0:1], 0xc0
	s_mov_b32 s94, s2
	s_add_u32 s2, s0, 0xd0
	s_addc_u32 s3, s1, 0
	v_mov_b32_e32 v1, v0
	v_writelane_b32 v254, s2, 0
	s_nop 0
	v_cmp_eq_u32_e32 vcc, 0, v1
	v_writelane_b32 v254, s3, 1
	s_and_saveexec_b64 s[2:3], vcc
	s_cbranch_execz .LBB0_2
	s_add_i32 s4, 0, 0x27ff0
	v_mov_b32_e32 v2, 0
	v_mov_b32_e32 v3, v2
	v_mov_b32_e32 v4, v2
	v_mov_b32_e32 v5, v2
	v_mov_b32_e32 v1, s4
	ds_write_b128 v1, v[2:5]

.LBB0_176:
	s_load_dwordx16 s[48:63], s[0:1], 0x40
	s_load_dwordx16 s[4:19], s[0:1], 0x80
	s_cmp_lt_i32 s90, 2
	s_cselect_b64 s[0:1], -1, 0
	s_add_u32 s96, s88, 0x35d10000
	s_addc_u32 s97, s89, 0
	s_waitcnt lgkmcnt(0)
	v_writelane_b32 v254, s4, 18
	s_and_b64 s[0:1], s[0:1], s[2:3]
	s_nop 0
	v_writelane_b32 v254, s5, 19
	v_writelane_b32 v254, s6, 20
	v_writelane_b32 v254, s7, 21
	v_writelane_b32 v254, s8, 22
	v_writelane_b32 v254, s9, 23
	v_writelane_b32 v254, s10, 24
	v_writelane_b32 v254, s11, 25
	v_writelane_b32 v254, s12, 26
	v_writelane_b32 v254, s13, 27
	v_writelane_b32 v254, s14, 28
	v_writelane_b32 v254, s15, 29
	v_writelane_b32 v254, s16, 30
	v_writelane_b32 v254, s17, 31
	v_writelane_b32 v254, s18, 32
	v_writelane_b32 v254, s19, 33
	v_writelane_b32 v254, s0, 34
	s_andn2_b64 vcc, exec, s[0:1]
	s_nop 0
	v_writelane_b32 v254, s1, 35
	s_cbranch_vccnz .LBB0_497
	s_cmpk_lg_i32 s92, 0x100
	s_cselect_b32 s33, s92, 0x100
	s_cmp_ge_i32 s94, s33
	s_cbranch_scc1 .LBB0_193
	s_abs_i32 s0, s33
	v_cvt_f32_u32_e32 v2, s0
	s_add_i32 s1, s33, 0x4bf
	s_sub_i32 s2, 0xfffffb41, s33
	s_xor_b32 s3, s1, s33
	v_rcp_iflag_f32_e32 v2, v2
	s_max_i32 s1, s1, s2
	s_sub_i32 s2, 0, s0
	s_ashr_i32 s3, s3, 31
	v_mul_f32_e32 v2, 0x4f7ffffe, v2
	v_cvt_u32_f32_e32 v2, v2
	v_mov_b32_e32 v1, v0
	v_readfirstlane_b32 s4, v2
	s_mul_i32 s2, s2, s4
	s_mul_hi_u32 s2, s4, s2
	s_add_i32 s4, s4, s2
	s_mul_hi_u32 s2, s1, s4
	s_mul_i32 s4, s2, s0
	s_sub_i32 s1, s1, s4
	s_add_i32 s4, s2, 1
	s_sub_i32 s5, s1, s0
	s_cmp_ge_u32 s1, s0
	s_cselect_b32 s2, s4, s2
	s_cselect_b32 s1, s5, s1
	s_add_i32 s4, s2, 1
	s_cmp_ge_u32 s1, s0
	s_cselect_b32 s0, s4, s2
	s_xor_b32 s0, s0, s3
	s_sub_i32 s41, s0, s3
	s_cmp_lt_i32 s41, 1
	s_cselect_b64 s[0:1], -1, 0
	s_cmpk_gt_i32 s94, 0x4bf
	s_cselect_b64 s[2:3], -1, 0
	s_or_b64 s[0:1], s[2:3], s[0:1]
	v_readfirstlane_b32 s72, v1
	s_and_b64 vcc, exec, s[0:1]
	s_cbranch_vccnz .LBB0_193
	s_add_u32 s40, s88, 0x10000
	s_addc_u32 s46, s89, 0
	s_ashr_i32 s45, s94, 31
	s_lshr_b32 s0, s45, 29
	s_add_i32 s0, s94, s0
	s_ashr_i32 s21, s72, 6
	s_ashr_i32 s1, s0, 3
	s_and_b32 s0, s0, -8
	v_writelane_b32 v254, s93, 36
	s_ashr_i32 s22, s72, 8
	s_lshl_b32 s44, s21, 10
	s_mov_b32 s2, s94
	s_sub_i32 s0, s94, s0
	v_writelane_b32 v254, s2, 37
	s_cmp_lt_i32 s0, 0
	s_movk_i32 s73, 0x99
	v_writelane_b32 v254, s3, 38
	s_cselect_b32 s2, s73, 0x98
	s_mul_i32 s0, s2, s0
	s_add_i32 s0, s0, s1
	v_bfe_i32 v4, v1, 27, 1
	s_mul_hi_i32 s1, s0, 0x6bca1af3
	v_lshlrev_b32_e32 v3, 4, v1
	v_lshrrev_b32_e32 v4, 22, v4
	s_lshr_b32 s2, s1, 31
	s_ashr_i32 s1, s1, 6
	v_add_u32_e32 v4, v3, v4
	s_add_i32 s1, s1, s2
	v_and_b32_e32 v4, 0xfffffc00, v4
	s_lshl_b32 s2, s1, 3
	s_mulk_i32 s1, 0x98
	v_sub_u32_e32 v3, v3, v4
	s_sub_i32 s0, s0, s1
	v_lshrrev_b32_e32 v4, 4, v3
	s_sext_i32_i16 s1, s0
	v_bitop3_b32 v4, v4, v3, 32 bitop3:0x6c
	v_ashrrev_i32_e32 v3, 31, v3
	s_bfe_u32 s1, s1, 0x3001c
	v_lshrrev_b32_e32 v3, 26, v3
	s_add_i32 s1, s0, s1
	v_add_u32_e32 v3, v4, v3
	s_sext_i32_i16 s3, s1
	s_and_b32 s1, s1, 0xfff8
	v_ashrrev_i32_e32 v2, 31, v1
	v_ashrrev_i32_e32 v7, 6, v3
	s_sub_i32 s0, s0, s1
	v_lshrrev_b32_e32 v2, 26, v2
	v_mul_i32_i24_e32 v3, 64, v7
	s_sext_i32_i16 s0, s0
	v_add_u32_e32 v2, v1, v2
	v_sub_u32_e32 v3, v4, v3
	v_mov_b32_e32 v4, 1
	s_lshr_b32 s20, s3, 3
	s_add_i32 s30, s2, s0
	v_ashrrev_i32_e32 v6, 6, v2
	v_ashrrev_i16_sdwa v3, v4, sext(v3) dst_sel:DWORD dst_unused:UNUSED_PAD src0_sel:DWORD src1_sel:BYTE_0
	s_ashr_i32 s31, s30, 31
	s_bfe_i64 s[0:1], s[20:21], 0x100000
	v_lshlrev_b32_e32 v2, 5, v6
	v_bfe_i32 v8, v3, 0, 16
	v_lshlrev_b32_e32 v3, 3, v6
	s_lshl_b64 s[2:3], s[30:31], 20
	s_lshl_b64 s[0:1], s[0:1], 20
	v_and_b32_e32 v2, 32, v2
	v_and_b32_e32 v3, 0xffff0, v3
	s_add_u32 s36, s40, s0
	v_add_u32_e32 v2, v2, v8
	v_add_lshl_u32 v3, v7, v3, 12
	s_addc_u32 s37, s46, s1
	s_add_i32 s31, s44, 0
	v_lshl_add_u32 v130, v2, 1, v3
	v_mov_b32_e32 v133, 0
	s_add_i32 m0, s31, 0x10000
	v_mov_b32_e32 v131, v133
	global_load_lds_dwordx4 v130, s[36:37]
	s_add_i32 m0, s31, 0x12000
	v_lshl_add_u64 v[2:3], s[36:37], 0, v[130:131]
	s_mov_b64 s[0:1], 0x40000
	s_add_u32 s34, s96, s2
	v_lshl_add_u64 v[4:5], v[2:3], 0, s[0:1]
	s_addc_u32 s35, s97, s3
	global_load_lds_dwordx4 v[4:5], off
	v_lshl_add_u64 v[4:5], s[34:35], 0, v[130:131]
	s_mov_b32 m0, s31
	s_add_i32 s47, s31, 0x2000
	global_load_lds_dwordx4 v130, s[34:35]
	v_lshl_add_u64 v[10:11], v[4:5], 0, s[0:1]
	s_mov_b32 m0, s47
	s_mov_b64 s[2:3], 0x80000
	global_load_lds_dwordx4 v[10:11], off
	v_lshl_add_u64 v[10:11], v[2:3], 0, s[2:3]
	s_add_i32 m0, s31, 0x14000
	s_mov_b64 s[4:5], 0xc0000
	global_load_lds_dwordx4 v[10:11], off
	v_lshl_add_u64 v[10:11], v[2:3], 0, s[4:5]
	s_add_i32 m0, s31, 0x16000
	s_add_i32 s64, s31, 0x4000
	global_load_lds_dwordx4 v[10:11], off
	v_lshl_add_u64 v[10:11], v[4:5], 0, s[2:3]
	s_mov_b32 m0, s64
	s_add_i32 s65, s31, 0x6000
	global_load_lds_dwordx4 v[10:11], off
	v_lshl_add_u64 v[10:11], v[4:5], 0, s[4:5]
	s_mov_b32 m0, s65
	s_cmp_lg_u32 s22, 1
	global_load_lds_dwordx4 v[10:11], off
	s_cbranch_scc1 .LBB0_181
	s_barrier

.LBB0_251:
	s_or_b64 exec, exec, s[2:3]
	s_cmp_lg_u32 s100, 0
	s_cbranch_scc1 .Lcq_go
	s_branch .LBB0_497
.Lcq_go:
	s_add_u32 s0, s88, 0x4200
	v_mov_b32_e32 v1, v0
	s_addc_u32 s1, s89, 0
	s_waitcnt vmcnt(0)
	s_barrier
	s_nop 0
	v_cmp_eq_u32_e32 vcc, 0, v1
	s_and_saveexec_b64 s[2:3], vcc
	s_cbranch_execz .LBB0_259
	s_mov_b64 s[6:7], exec
	v_mbcnt_lo_u32_b32 v1, s6, 0
	v_mbcnt_hi_u32_b32 v1, s7, v1
	v_cmp_eq_u32_e32 vcc, 0, v1
	s_and_saveexec_b64 s[4:5], vcc
	s_cbranch_execz .LBB0_254
	s_bcnt1_i32_b64 s6, s[6:7]
	v_mov_b32_e32 v2, 0
	v_mov_b32_e32 v3, s6
	global_atomic_add v2, v2, v3, s[0:1] sc0

.LBB0_409:
	s_or_b64 exec, exec, s[6:7]
	v_mov_b32_e32 v126, 0
	v_mov_b32_e32 v125, 0
	v_mov_b32_e32 v124, 0
	v_mov_b32_e32 v127, 0
	v_mov_b32_e32 v69, 0
	v_mov_b32_e32 v68, 0
	v_mov_b32_e32 v67, 0
	v_mov_b32_e32 v66, 0
	s_and_saveexec_b64 s[6:7], vcc
	s_cbranch_execz .LBB0_411
	v_mad_u64_u32 v[50:51], s[8:9], v74, 24, v[70:71]
	v_lshl_add_u64 v[52:53], v[74:75], 2, v[50:51]
	global_load_dwordx4 v[124:127], v[50:51], off
	global_load_dwordx4 v[66:69], v[52:53], off

.LBB0_412:
	s_or_b64 exec, exec, s[2:3]
	s_add_u32 s74, s88, 0x25b10000
	s_addc_u32 s75, s89, 0
	s_add_u32 s76, s88, 0x5b10000
	s_addc_u32 s77, s89, 0
	s_add_u32 s78, s88, 0x4b10000
	s_addc_u32 s79, s89, 0
	s_add_u32 s80, s88, 0x2b10000
	s_addc_u32 s81, s89, 0
	s_add_u32 s82, s88, 0x1b10000
	s_addc_u32 s83, s89, 0
	s_add_u32 s84, s88, 0x1310000
	s_addc_u32 s85, s89, 0
	s_add_u32 s20, s88, 0x10000
	v_readlane_b32 s4, v254, 18
	s_addc_u32 s21, s89, 0
	v_readlane_b32 s16, v254, 30
	v_readlane_b32 s17, v254, 31
	v_readlane_b32 s6, v254, 20
	v_readlane_b32 s7, v254, 21
	s_cmp_lg_u64 s[16:17], 0
	s_cselect_b64 s[24:25], -1, 0
	s_cmp_lg_u64 s[6:7], 0
	s_cselect_b64 s[26:27], -1, 0
	s_add_u32 s28, s62, 0x4000
	s_addc_u32 s29, s63, 0
	s_cmp_lg_u64 s[62:63], 0
	s_mov_b64 s[2:3], src_shared_base
	s_cselect_b64 s[30:31], -1, 0
	s_cmp_lg_u64 s[60:61], 0
	s_mov_b64 s[22:23], 0
	s_mov_b32 s2, 3
	s_cselect_b64 s[34:35], -1, 0
	v_mov_b32_e32 v71, 0
	s_movk_i32 s33, 0xfc
	s_mov_b32 s68, 0xc000
	v_mov_b32_e32 v51, 0x7fffed00
	v_mov_b64_e32 v[52:53], v[106:107]
	v_mov_b32_e32 v110, v108
	v_mov_b32_e32 v119, v109
	v_readlane_b32 s5, v254, 19
	v_readlane_b32 s8, v254, 22
	v_readlane_b32 s9, v254, 23
	v_readlane_b32 s10, v254, 24
	v_readlane_b32 s11, v254, 25
	v_readlane_b32 s12, v254, 26
	v_readlane_b32 s13, v254, 27
	v_readlane_b32 s14, v254, 28
	v_readlane_b32 s15, v254, 29
	v_readlane_b32 s18, v254, 32
	v_readlane_b32 s19, v254, 33
	s_mov_b32 s98, 0
	v_mov_b32_e32 v70, v0
	s_nop 0
	v_cmp_eq_u32_e32 vcc, 0, v70
	s_and_saveexec_b64 s[36:37], vcc
	s_cbranch_execz .Lcvp_noat
	v_mov_b32_e32 v200, 1
	global_atomic_add v200, v71, v200, s[0:1] sc0
.Lcvp_noat:
	s_or_b64 exec, exec, s[36:37]
	s_branch .Lcv0_414
.Lcv0_414:
	v_mov_b32_e32 v70, v0
	v_mov_b32_e32 v65, v111
	v_mov_b32_e32 v118, v114
	v_mov_b64_e32 v[112:113], v[72:73]
	s_nop 0
	v_cmp_eq_u32_e32 vcc, 0, v70
	s_and_saveexec_b64 s[36:37], vcc
	s_cbranch_execz .Lcv0_418
	s_cmp_eq_u32 s98, 0
	s_cbranch_scc1 .Lcv0_415
	s_waitcnt vmcnt(10)
	s_branch .Lcv0_416

.Lcv0_416:
	v_add_u32_e32 v70, 0x260, v200
	s_and_b32 s8, s2, 3
	s_lshl_b32 s8, s8, 2
	s_add_i32 s8, s8, 0xa000
	v_mov_b32_e32 v114, s8
	ds_write_b32 v114, v70
	v_mov_b32_e32 v200, 1
	global_atomic_add v200, v71, v200, s[0:1] sc0
.Lcv0_418:
	s_or_b64 exec, exec, s[36:37]
	s_add_i32 s8, s2, -3
	s_and_b32 s8, s8, 3
	s_xor_b32 s8, s8, 2
	s_lshl_b32 s8, s8, 2
	s_add_i32 s8, s8, 0xa000
	v_mov_b32_e32 v72, s8
	ds_read_b32 v120, v72
	s_movk_i32 s8, 0x6b60
	s_waitcnt lgkmcnt(0)
	v_cmp_gt_i32_e32 vcc, s8, v120
	s_and_saveexec_b64 s[36:37], vcc
	s_cbranch_execz .Lcv0_417
	s_movk_i32 s8, 0x25f
	v_cmp_lt_i32_e32 vcc, s8, v120
	s_and_saveexec_b64 s[8:9], vcc
	s_xor_b64 s[38:39], exec, s[8:9]
	s_cbranch_execz .Lcv0_459
	s_movk_i32 s8, 0x35f
	v_cmp_lt_u32_e32 vcc, s8, v120
	s_and_saveexec_b64 s[8:9], vcc
	s_xor_b64 s[40:41], exec, s[8:9]
	s_cbranch_execz .Lcv0_453
	s_movk_i32 s8, 0x95f
	v_cmp_lt_u32_e32 vcc, s8, v120
	s_and_saveexec_b64 s[8:9], vcc
	s_xor_b64 s[42:43], exec, s[8:9]
	s_cbranch_execz .Lcv0_441
	s_movk_i32 s8, 0xb5f
	v_cmp_lt_u32_e32 vcc, s8, v120
	s_and_saveexec_b64 s[8:9], vcc
	s_xor_b64 s[44:45], exec, s[8:9]
	s_cbranch_execz .Lcv0_434
	s_movk_i32 s8, 0x4b5f
	v_cmp_lt_u32_e32 vcc, s8, v120
	s_and_saveexec_b64 s[8:9], vcc
	s_xor_b64 s[46:47], exec, s[8:9]
	s_cbranch_execz .Lcv0_428
	v_add_u32_e32 v72, 0xffffb4a0, v120
	v_lshrrev_b32_e32 v70, 6, v72
	v_lshlrev_b32_e32 v72, 5, v72
	v_and_b32_e32 v74, 0x700, v72
	v_lshlrev_b32_e32 v72, 6, v120
	v_and_b32_e32 v72, 0x1c0, v72
	v_mov_b32_e32 v73, v0
	s_andn2_b64 vcc, exec, s[24:25]
	s_cbranch_vccnz .Lcv0_426
	v_readlane_b32 s4, v254, 18
	v_lshlrev_b32_e32 v75, 2, v73
	v_lshlrev_b64 v[76:77], 22, v[70:71]
	v_readlane_b32 s16, v254, 30
	v_readlane_b32 s17, v254, 31
	v_and_or_b32 v75, v75, s33, v74
	v_ashrrev_i32_e32 v73, 3, v73
	v_lshl_add_u64 v[76:77], s[16:17], 0, v[76:77]
	v_lshlrev_b32_e32 v78, 2, v75
	v_mov_b32_e32 v79, v71
	v_and_b32_e32 v73, -8, v73
	v_lshl_add_u64 v[76:77], v[76:77], 0, v[78:79]
	v_add_u32_e32 v78, v73, v72
	v_ashrrev_i32_e32 v79, 31, v78
	v_lshlrev_b64 v[78:79], 13, v[78:79]
	v_lshl_add_u64 v[114:115], v[76:77], 0, v[78:79]
	v_readlane_b32 s5, v254, 19
	v_readlane_b32 s6, v254, 20
	v_readlane_b32 s7, v254, 21
	v_readlane_b32 s8, v254, 22
	v_readlane_b32 s9, v254, 23
	v_readlane_b32 s10, v254, 24
	v_readlane_b32 s11, v254, 25
	v_readlane_b32 s12, v254, 26
	v_readlane_b32 s13, v254, 27
	v_readlane_b32 s14, v254, 28
	v_readlane_b32 s15, v254, 29
	v_readlane_b32 s18, v254, 32
	v_readlane_b32 s19, v254, 33
	s_branch .Lcv0_427

.Lcv0_491:
	s_or_b64 exec, exec, s[38:39]
	s_waitcnt vmcnt(16)
	s_mov_b32 s98, 1
	s_branch .Lcv0_492
.Lcv0_417:
	s_waitcnt vmcnt(0)
	s_mov_b32 s98, 0

.Lcv0_413:
	s_or_b64 exec, exec, s[36:37]
	s_movk_i32 s8, 0x6b5f
	v_cmp_lt_i32_e32 vcc, s8, v1
	s_add_i32 s2, s2, 1
	s_or_b64 s[22:23], vcc, s[22:23]
	v_mov_b32_e32 v1, v120
	v_mov_b64_e32 v[72:73], v[106:107]
	v_mov_b32_e32 v114, v108
	v_mov_b32_e32 v111, v109
	v_mov_b64_e32 v[52:53], v[112:113]
	v_mov_b32_e32 v110, v118
	v_mov_b32_e32 v119, v65
	s_barrier
	s_andn2_b64 exec, exec, s[22:23]
	s_cbranch_execz .LBB0_496

.Lcv1_418:
	s_or_b64 exec, exec, s[36:37]
	s_add_i32 s8, s2, -3
	s_and_b32 s8, s8, 3
	s_xor_b32 s8, s8, 2
	s_lshl_b32 s8, s8, 2
	s_add_i32 s8, s8, 0xa000
	v_mov_b32_e32 v72, s8
	ds_read_b32 v120, v72
	s_movk_i32 s8, 0x6b60
	s_waitcnt lgkmcnt(0)
	v_cmp_gt_i32_e32 vcc, s8, v120
	s_and_saveexec_b64 s[36:37], vcc
	s_cbranch_execz .Lcv1_417
	s_movk_i32 s8, 0x25f
	v_cmp_lt_i32_e32 vcc, s8, v120
	s_and_saveexec_b64 s[8:9], vcc
	s_xor_b64 s[38:39], exec, s[8:9]
	s_cbranch_execz .Lcv1_459
	s_movk_i32 s8, 0x35f
	v_cmp_lt_u32_e32 vcc, s8, v120
	s_and_saveexec_b64 s[8:9], vcc
	s_xor_b64 s[40:41], exec, s[8:9]
	s_cbranch_execz .Lcv1_453
	s_movk_i32 s8, 0x95f
	v_cmp_lt_u32_e32 vcc, s8, v120
	s_and_saveexec_b64 s[8:9], vcc
	s_xor_b64 s[42:43], exec, s[8:9]
	s_cbranch_execz .Lcv1_441
	s_movk_i32 s8, 0xb5f
	v_cmp_lt_u32_e32 vcc, s8, v120
	s_and_saveexec_b64 s[8:9], vcc
	s_xor_b64 s[44:45], exec, s[8:9]
	s_cbranch_execz .Lcv1_434
	s_movk_i32 s8, 0x4b5f
	v_cmp_lt_u32_e32 vcc, s8, v120
	s_and_saveexec_b64 s[8:9], vcc
	s_xor_b64 s[46:47], exec, s[8:9]
	s_cbranch_execz .Lcv1_428
	v_add_u32_e32 v72, 0xffffb4a0, v120
	v_lshrrev_b32_e32 v70, 6, v72
	v_lshlrev_b32_e32 v72, 5, v72
	v_and_b32_e32 v2, 0x700, v72
	v_lshlrev_b32_e32 v72, 6, v120
	v_and_b32_e32 v72, 0x1c0, v72
	v_mov_b32_e32 v73, v0
	s_andn2_b64 vcc, exec, s[24:25]
	s_cbranch_vccnz .Lcv1_426
	v_readlane_b32 s4, v254, 18
	v_lshlrev_b32_e32 v3, 2, v73
	v_lshlrev_b64 v[4:5], 22, v[70:71]
	v_readlane_b32 s16, v254, 30
	v_readlane_b32 s17, v254, 31
	v_and_or_b32 v3, v3, s33, v2
	v_ashrrev_i32_e32 v73, 3, v73
	v_lshl_add_u64 v[4:5], s[16:17], 0, v[4:5]
	v_lshlrev_b32_e32 v10, 2, v3
	v_mov_b32_e32 v11, v71
	v_and_b32_e32 v73, -8, v73
	v_lshl_add_u64 v[4:5], v[4:5], 0, v[10:11]
	v_add_u32_e32 v10, v73, v72
	v_ashrrev_i32_e32 v11, 31, v10
	v_lshlrev_b64 v[10:11], 13, v[10:11]
	v_lshl_add_u64 v[114:115], v[4:5], 0, v[10:11]
	v_readlane_b32 s5, v254, 19
	v_readlane_b32 s6, v254, 20
	v_readlane_b32 s7, v254, 21
	v_readlane_b32 s8, v254, 22
	v_readlane_b32 s9, v254, 23
	v_readlane_b32 s10, v254, 24
	v_readlane_b32 s11, v254, 25
	v_readlane_b32 s12, v254, 26
	v_readlane_b32 s13, v254, 27
	v_readlane_b32 s14, v254, 28
	v_readlane_b32 s15, v254, 29
	v_readlane_b32 s18, v254, 32
	v_readlane_b32 s19, v254, 33
	s_branch .Lcv1_427

.Lcv1_427:
	v_lshlrev_b64 v[4:5], 20, v[70:71]
	v_mov_b32_e32 v70, v0
	v_lshl_add_u64 v[4:5], s[74:75], 0, v[4:5]
	v_ashrrev_i32_e32 v3, 2, v70
	v_add_u32_e32 v2, v3, v2
	v_ashrrev_i32_e32 v3, 31, v2
	v_lshlrev_b64 v[2:3], 9, v[2:3]
	v_mov_b32_e32 v73, v71
	v_lshl_add_u64 v[2:3], v[4:5], 0, v[2:3]
	v_lshlrev_b32_e32 v70, 4, v70
	v_lshl_add_u64 v[72:73], v[2:3], 0, v[72:73]
	v_and_b32_e32 v70, 48, v70
	v_lshl_add_u64 v[106:107], v[72:73], 0, v[70:71]
.Lcv1_428:
	s_or_saveexec_b64 s[46:47], s[46:47]
	v_mov_b64_e32 v[116:117], 0x800
	v_mov_b32_e32 v108, 0x200
	v_mov_b32_e32 v109, 0x41800000
	s_xor_b64 exec, exec, s[46:47]
	s_cbranch_execz .Lcv1_437
	v_add_u32_e32 v12, 0xfffff4a0, v120
	v_mov_b32_e32 v13, v0
	v_lshlrev_b32_e32 v73, 2, v12
	v_lshlrev_b32_e32 v72, 2, v13
	v_lshrrev_b32_e32 v70, 7, v12
	v_and_b32_e32 v72, 0xfc, v72
	s_movk_i32 s8, 0x7f
	v_and_b32_e32 v73, 0x180, v73
	v_lshlrev_b64 v[2:3], 20, v[70:71]
	v_cmp_lt_u32_e32 vcc, s8, v72
	v_lshlrev_b32_e32 v4, 2, v73
	v_lshlrev_b32_e32 v72, 2, v72
	s_and_saveexec_b64 s[8:9], vcc
	s_xor_b64 s[64:65], exec, s[8:9]
	s_cbranch_execz .Lcv1_431
	v_readlane_b32 s4, v254, 18
	v_readlane_b32 s14, v254, 28
	v_readlane_b32 s15, v254, 29
	v_readlane_b32 s8, v254, 22
	v_readlane_b32 s9, v254, 23
	v_lshl_add_u64 v[2:3], v[2:3], 2, s[14:15]
	v_mov_b32_e32 v5, v71
	v_lshl_add_u64 v[2:3], v[2:3], 0, v[4:5]
	v_mov_b32_e32 v73, v71
	s_movk_i32 s8, 0xfe00
	v_lshl_add_u64 v[72:73], v[2:3], 0, v[72:73]
	s_mov_b32 s9, -1
	v_readlane_b32 s5, v254, 19
	v_readlane_b32 s6, v254, 20
	v_readlane_b32 s7, v254, 21
	v_readlane_b32 s10, v254, 24
	v_readlane_b32 s11, v254, 25
	v_readlane_b32 s12, v254, 26
	v_readlane_b32 s13, v254, 27
	v_readlane_b32 s16, v254, 30
	v_readlane_b32 s17, v254, 31
	v_readlane_b32 s18, v254, 32
	v_readlane_b32 s19, v254, 33
	v_lshl_add_u64 v[10:11], v[72:73], 0, s[8:9]
.Lcv1_431:
	s_andn2_saveexec_b64 s[64:65], s[64:65]
	s_cbranch_execz .Lcv1_433
	v_readlane_b32 s4, v254, 18
	v_readlane_b32 s12, v254, 26
	v_readlane_b32 s13, v254, 27
	v_mov_b32_e32 v5, v71
	v_mov_b32_e32 v73, v71
	v_lshl_add_u64 v[2:3], v[2:3], 2, s[12:13]
	v_lshl_add_u64 v[2:3], v[2:3], 0, v[4:5]
	v_lshl_add_u64 v[10:11], v[2:3], 0, v[72:73]
	v_readlane_b32 s5, v254, 19
	v_readlane_b32 s6, v254, 20
	v_readlane_b32 s7, v254, 21
	v_readlane_b32 s8, v254, 22
	v_readlane_b32 s9, v254, 23
	v_readlane_b32 s10, v254, 24
	v_readlane_b32 s11, v254, 25
	v_readlane_b32 s14, v254, 28
	v_readlane_b32 s15, v254, 29
	v_readlane_b32 s16, v254, 30
	v_readlane_b32 s17, v254, 31
	v_readlane_b32 s18, v254, 32
	v_readlane_b32 s19, v254, 33
.Lcv1_433:
	s_or_b64 exec, exec, s[64:65]
	v_lshlrev_b64 v[72:73], 21, v[70:71]
	v_lshlrev_b32_e32 v70, 3, v12
	v_and_b32_e32 v4, 0x300, v70
	v_lshlrev_b32_e32 v70, 6, v120
	v_ashrrev_i32_e32 v2, 3, v13
	v_and_b32_e32 v70, 0x7c0, v70
	v_and_b32_e32 v2, -8, v2
	v_add_u32_e32 v2, v2, v70
	v_ashrrev_i32_e32 v3, 31, v2
	v_lshlrev_b64 v[2:3], 11, v[2:3]
	v_lshl_add_u64 v[2:3], v[10:11], 0, v[2:3]
	v_cmp_ne_u64_e32 vcc, 0, v[10:11]
	v_mov_b32_e32 v5, v0
	v_lshl_add_u64 v[72:73], s[76:77], 0, v[72:73]
	v_cndmask_b32_e32 v114, 0, v2, vcc
	v_ashrrev_i32_e32 v2, 2, v5
	v_add_u32_e32 v2, v2, v4
	v_cndmask_b32_e32 v115, 0, v3, vcc
	v_ashrrev_i32_e32 v3, 31, v2
	v_lshlrev_b64 v[2:3], 11, v[2:3]
	v_lshl_add_u64 v[72:73], v[72:73], 0, v[2:3]
	v_lshl_add_u64 v[72:73], v[72:73], 0, v[70:71]
	v_lshlrev_b32_e32 v70, 4, v5
	v_and_b32_e32 v70, 48, v70
	v_lshl_add_u64 v[106:107], v[72:73], 0, v[70:71]
	v_mov_b64_e32 v[116:117], 0x200
	v_mov_b32_e32 v108, 0x800
	v_mov_b32_e32 v109, 0x42000000
	s_or_b64 exec, exec, s[46:47]

.Lcv1_435:
	v_add_u32_e32 v70, 0xfffff6a0, v120
	v_lshlrev_b32_e32 v72, 2, v70
	v_lshlrev_b32_e32 v70, 6, v70
	v_and_b32_e32 v72, 0x7fffff00, v72
	v_and_b32_e32 v70, 0xfc0, v70
	v_mov_b32_e32 v73, v0
	s_andn2_b64 vcc, exec, s[26:27]
	s_cbranch_vccnz .Lcv1_438
	v_lshlrev_b32_e32 v2, 2, v73
	v_ashrrev_i32_e32 v73, 3, v73
	v_and_b32_e32 v73, -8, v73
	v_readlane_b32 s4, v254, 18
	v_add_u32_e32 v4, v73, v70
	v_and_or_b32 v2, v2, s33, v72
	v_mov_b32_e32 v3, v71
	v_readlane_b32 s6, v254, 20
	v_readlane_b32 s7, v254, 21
	v_ashrrev_i32_e32 v5, 31, v4
	v_lshlrev_b64 v[4:5], 13, v[4:5]
	v_lshl_add_u64 v[2:3], v[2:3], 2, s[6:7]
	v_lshl_add_u64 v[114:115], v[2:3], 0, v[4:5]
	v_readlane_b32 s5, v254, 19
	v_readlane_b32 s8, v254, 22
	v_readlane_b32 s9, v254, 23
	v_readlane_b32 s10, v254, 24
	v_readlane_b32 s11, v254, 25
	v_readlane_b32 s12, v254, 26
	v_readlane_b32 s13, v254, 27
	v_readlane_b32 s14, v254, 28
	v_readlane_b32 s15, v254, 29
	v_readlane_b32 s16, v254, 30
	v_readlane_b32 s17, v254, 31
	v_readlane_b32 s18, v254, 32
	v_readlane_b32 s19, v254, 33
	s_branch .Lcv1_439

.Lcv1_439:
	v_mov_b32_e32 v2, v0
	v_mov_b64_e32 v[116:117], 0x800
	v_ashrrev_i32_e32 v73, 2, v2
	v_add_u32_e32 v72, v73, v72
	v_ashrrev_i32_e32 v73, 31, v72
	v_lshlrev_b64 v[72:73], 12, v[72:73]
	v_lshl_add_u64 v[72:73], s[78:79], 0, v[72:73]
	v_lshl_add_u64 v[72:73], v[72:73], 0, v[70:71]
	v_lshlrev_b32_e32 v70, 4, v2
	v_and_b32_e32 v70, 48, v70
	v_lshl_add_u64 v[106:107], v[72:73], 0, v[70:71]
	v_mov_b32_e32 v108, 0x1000
	v_mov_b32_e32 v109, 0x42800000

.Lcv1_441:
	s_andn2_saveexec_b64 s[42:43], s[42:43]
	s_cbranch_execz .Lcv1_452
	v_add_u32_e32 v70, 0xfffffca0, v120
	s_movk_i32 s8, 0x1ff
	v_cmp_lt_u32_e32 vcc, s8, v70
	v_lshlrev_b32_e32 v70, 3, v70
	v_and_b32_e32 v72, 0x7fffff00, v70
	s_and_saveexec_b64 s[8:9], vcc
	s_xor_b64 s[44:45], exec, s[8:9]
	s_cbranch_execz .Lcv1_446
	v_add_u32_e32 v72, 0xfffff000, v72
	v_lshlrev_b32_e32 v70, 6, v120
	s_movk_i32 s8, 0x2000
	v_and_b32_e32 v70, 0x7c0, v70
	v_mov_b32_e32 v73, v0
	v_cmp_gt_u32_e32 vcc, s8, v72
	v_mov_b64_e32 v[114:115], 0
	s_and_saveexec_b64 s[46:47], vcc
	v_lshlrev_b32_e32 v2, 2, v73
	v_ashrrev_i32_e32 v73, 3, v73
	v_and_or_b32 v2, v2, s33, v72
	v_mov_b32_e32 v3, v71
	v_and_b32_e32 v73, -8, v73
	v_lshl_add_u64 v[2:3], v[2:3], 2, s[28:29]
	v_add_u32_e32 v73, v73, v70
	v_mad_i64_i32 v[114:115], s[8:9], v73, s68, v[2:3]
	s_or_b64 exec, exec, s[46:47]
	v_mov_b32_e32 v2, v0
	s_nop 0
	v_ashrrev_i32_e32 v73, 2, v2
	v_add_u32_e32 v72, v73, v72
	v_ashrrev_i32_e32 v73, 31, v72
	v_lshlrev_b64 v[72:73], 11, v[72:73]
	v_lshl_add_u64 v[72:73], s[80:81], 0, v[72:73]
	v_lshl_add_u64 v[72:73], v[72:73], 0, v[70:71]
	v_lshlrev_b32_e32 v70, 4, v2
	v_and_b32_e32 v70, 48, v70
	v_lshl_add_u64 v[106:107], v[72:73], 0, v[70:71]
.Lcv1_446:
	s_andn2_saveexec_b64 s[44:45], s[44:45]
	s_cbranch_execz .Lcv1_451
	v_lshlrev_b32_e32 v70, 6, v120
	v_and_b32_e32 v70, 0x7c0, v70
	v_mov_b32_e32 v73, v0
	s_andn2_b64 vcc, exec, s[30:31]
	s_cbranch_vccnz .Lcv1_449
	v_lshlrev_b32_e32 v2, 2, v73
	v_ashrrev_i32_e32 v73, 3, v73
	v_and_or_b32 v2, v2, s33, v72
	v_mov_b32_e32 v3, v71
	v_and_b32_e32 v73, -8, v73
	v_lshl_add_u64 v[2:3], v[2:3], 2, s[62:63]
	v_add_u32_e32 v73, v73, v70
	v_mad_i64_i32 v[114:115], s[8:9], v73, s68, v[2:3]
	s_branch .Lcv1_450

.Lcv1_450:
	v_mov_b32_e32 v2, v0
	s_nop 0
	v_ashrrev_i32_e32 v73, 2, v2
	v_add_u32_e32 v72, v73, v72
	v_ashrrev_i32_e32 v73, 31, v72
	v_lshlrev_b64 v[72:73], 11, v[72:73]
	v_lshl_add_u64 v[72:73], s[82:83], 0, v[72:73]
	v_lshl_add_u64 v[72:73], v[72:73], 0, v[70:71]
	v_lshlrev_b32_e32 v70, 4, v2
	v_and_b32_e32 v70, 48, v70
	v_lshl_add_u64 v[106:107], v[72:73], 0, v[70:71]

.Lcv1_453:
	s_andn2_saveexec_b64 s[40:41], s[40:41]
	s_cbranch_execz .Lcv1_458
	v_lshl_add_u32 v70, v120, 3, v51
	v_and_b32_e32 v2, 0x7fffff00, v70
	v_lshlrev_b32_e32 v70, 6, v120
	v_and_b32_e32 v73, 0x7c0, v70
	v_mov_b32_e32 v72, v0
	s_andn2_b64 vcc, exec, s[34:35]
	s_cbranch_vccnz .Lcv1_456
	v_lshlrev_b32_e32 v70, 2, v72
	v_and_or_b32 v70, v70, s33, v2
	v_lshl_add_u64 v[4:5], v[70:71], 2, s[60:61]
	v_ashrrev_i32_e32 v70, 3, v72
	v_and_b32_e32 v70, -8, v70
	v_add_u32_e32 v10, v70, v73
	v_ashrrev_i32_e32 v11, 31, v10
	v_lshlrev_b64 v[10:11], 13, v[10:11]
	v_lshl_add_u64 v[114:115], v[4:5], 0, v[10:11]
	s_branch .Lcv1_457

.Lcv1_457:
	v_ashrrev_i32_e32 v70, 2, v72
	v_add_u32_e32 v2, v70, v2
	v_ashrrev_i32_e32 v3, 31, v2
	v_lshlrev_b64 v[2:3], 12, v[2:3]
	v_lshl_add_u64 v[2:3], s[84:85], 0, v[2:3]
	v_lshlrev_b32_e32 v70, 1, v73
	v_lshl_add_u64 v[2:3], v[2:3], 0, v[70:71]
	v_lshlrev_b32_e32 v70, 5, v72
	v_and_b32_e32 v70, 0x60, v70
	v_lshl_add_u64 v[106:107], v[2:3], 0, v[70:71]
	v_mov_b64_e32 v[116:117], 0x800
	v_mov_b32_e32 v108, 0x800
	v_mov_b32_e32 v109, 0

.Lcv1_459:
	s_andn2_saveexec_b64 s[38:39], s[38:39]
	s_cbranch_execz .Lcv1_483
	v_ashrrev_i32_e32 v70, 31, v120
	v_lshrrev_b32_e32 v70, 27, v70
	v_add_u32_e32 v70, v120, v70
	v_ashrrev_i32_e32 v5, 5, v70
	v_mov_b32_e32 v70, v0
	v_lshlrev_b32_e32 v4, 8, v5
	s_movk_i32 s8, 0x7ff
	v_lshlrev_b32_e32 v72, 2, v70
	v_and_or_b32 v72, v72, s33, v4
	v_cmp_lt_i32_e32 vcc, s8, v72
	s_mov_b64 s[42:43], -1
	s_and_saveexec_b64 s[40:41], vcc
	s_cbranch_execz .Lcv1_478
	s_movk_i32 s8, 0xbff
	v_cmp_lt_u32_e32 vcc, s8, v4
	s_mov_b64 s[44:45], 0
	s_and_saveexec_b64 s[8:9], vcc
	s_xor_b64 s[42:43], exec, s[8:9]
	s_cbranch_execz .Lcv1_475
	s_movk_i32 s8, 0x11ff
	v_cmp_lt_u32_e32 vcc, s8, v4
	s_mov_b64 s[46:47], 0
	s_and_saveexec_b64 s[8:9], vcc
	s_xor_b64 s[44:45], exec, s[8:9]
	s_cbranch_execz .Lcv1_472
	s_movk_i32 s8, 0x123f
	v_cmp_lt_u32_e32 vcc, s8, v72
	s_mov_b64 s[64:65], 0
	s_and_saveexec_b64 s[8:9], vcc
	s_xor_b64 s[46:47], exec, s[8:9]
	s_cbranch_execz .Lcv1_469
	s_movk_i32 s8, 0x1247
	v_cmp_lt_u32_e32 vcc, s8, v72
	s_and_saveexec_b64 s[8:9], vcc
	s_xor_b64 s[66:67], exec, s[8:9]
	s_movk_i32 s8, 0x1258
	v_cmp_gt_u32_e32 vcc, s8, v72
	s_and_b64 s[64:65], vcc, exec
	s_andn2_saveexec_b64 s[66:67], s[66:67]
	v_add_u32_e32 v72, 0xfffff600, v72
	s_or_b64 s[64:65], s[64:65], exec
	s_or_b64 exec, exec, s[66:67]
	s_and_b64 s[64:65], s[64:65], exec

.Lcv1_478:
	s_or_b64 exec, exec, s[40:41]
	v_mov_b64_e32 v[114:115], 0
	v_mov_b64_e32 v[2:3], 0
	s_and_saveexec_b64 s[40:41], s[42:43]
	s_cbranch_execz .Lcv1_480
	v_readlane_b32 s4, v254, 2
	v_ashrrev_i32_e32 v73, 31, v72
	v_readlane_b32 s12, v254, 10
	v_readlane_b32 s13, v254, 11
	v_readlane_b32 s5, v254, 3
	v_readlane_b32 s6, v254, 4
	v_lshl_add_u64 v[2:3], v[72:73], 2, s[12:13]
	v_readlane_b32 s7, v254, 5
	v_readlane_b32 s8, v254, 6
	v_readlane_b32 s9, v254, 7
	v_readlane_b32 s10, v254, 8
	v_readlane_b32 s11, v254, 9
	v_readlane_b32 s14, v254, 12
	v_readlane_b32 s15, v254, 13
	v_readlane_b32 s16, v254, 14
	v_readlane_b32 s17, v254, 15
	v_readlane_b32 s18, v254, 16
	v_readlane_b32 s19, v254, 17
.Lcv1_480:
	s_or_b64 exec, exec, s[40:41]
	v_lshlrev_b32_e32 v72, 5, v5
	v_sub_u32_e32 v72, v120, v72
	v_lshlrev_b32_e32 v72, 6, v72
	v_cmp_ne_u64_e32 vcc, 0, v[2:3]
	s_and_saveexec_b64 s[40:41], vcc
	v_ashrrev_i32_e32 v73, 3, v70
	v_and_b32_e32 v73, -8, v73
	v_add_u32_e32 v73, v73, v72
	s_movk_i32 s8, 0x4960
	v_mad_i64_i32 v[114:115], s[8:9], v73, s8, v[2:3]
	s_or_b64 exec, exec, s[40:41]
	v_ashrrev_i32_e32 v73, 2, v70
	v_add_u32_e32 v2, v73, v4
	v_ashrrev_i32_e32 v3, 31, v2
	v_lshlrev_b64 v[2:3], 12, v[2:3]
	v_lshl_add_u64 v[2:3], s[20:21], 0, v[2:3]
	v_ashrrev_i32_e32 v73, 31, v72
	v_lshlrev_b32_e32 v70, 5, v70
	v_lshl_add_u64 v[72:73], v[72:73], 1, v[2:3]
	v_and_b32_e32 v70, 0x60, v70
	v_lshl_add_u64 v[106:107], v[72:73], 0, v[70:71]
	v_mov_b64_e32 v[116:117], 0x1258
	v_mov_b32_e32 v108, 0x800
	v_mov_b32_e32 v109, 0
.Lcv1_483:
	s_or_b64 exec, exec, s[38:39]
	v_mov_b32_e32 v4, v71
	v_mov_b32_e32 v5, v71
	v_mov_b32_e32 v2, v71
	v_mov_b32_e32 v3, v71
	v_mov_b64_e32 v[12:13], v[4:5]
	v_mov_b64_e32 v[8:9], v[4:5]
	v_cmp_ne_u64_e32 vcc, 0, v[114:115]
	v_mov_b64_e32 v[10:11], v[2:3]
	v_mov_b64_e32 v[6:7], v[2:3]
	s_and_saveexec_b64 s[38:39], vcc
	s_cbranch_execz .Lcv1_485
	v_lshl_add_u64 v[72:73], v[116:117], 2, v[114:115]
	global_load_dwordx4 v[10:13], v[114:115], off
	global_load_dwordx4 v[6:9], v[72:73], off
.Lcv1_485:
	s_or_b64 exec, exec, s[38:39]
	v_mov_b64_e32 v[20:21], v[4:5]
	v_mov_b64_e32 v[18:19], v[2:3]
	s_and_saveexec_b64 s[38:39], vcc
	s_cbranch_execz .Lcv1_487
	v_lshl_add_u64 v[72:73], v[116:117], 3, v[114:115]
	v_lshl_add_u64 v[18:19], v[116:117], 2, v[72:73]
	global_load_dwordx4 v[2:5], v[72:73], off
	s_nop 0
	global_load_dwordx4 v[18:21], v[18:19], off
.Lcv1_487:
	s_or_b64 exec, exec, s[38:39]
	v_mov_b32_e32 v72, v71
	v_mov_b32_e32 v73, v71
	v_mov_b32_e32 v70, v71
	v_mov_b64_e32 v[16:17], v[72:73]
	v_mov_b64_e32 v[24:25], v[72:73]
	v_mov_b64_e32 v[14:15], v[70:71]
	v_mov_b64_e32 v[22:23], v[70:71]
	s_and_saveexec_b64 s[38:39], vcc
	s_cbranch_execz .Lcv1_489
	v_lshl_add_u64 v[72:73], v[116:117], 4, v[114:115]
	v_lshl_add_u64 v[22:23], v[116:117], 2, v[72:73]
	global_load_dwordx4 v[14:17], v[72:73], off
	s_nop 0
	global_load_dwordx4 v[22:25], v[22:23], off
.Lcv1_489:
	s_or_b64 exec, exec, s[38:39]
	v_mov_b32_e32 v33, 0
	v_mov_b32_e32 v32, 0
	v_mov_b32_e32 v31, 0
	v_mov_b32_e32 v30, 0
	v_mov_b32_e32 v29, 0
	v_mov_b32_e32 v28, 0
	v_mov_b32_e32 v27, 0
	v_mov_b32_e32 v26, 0
	s_and_saveexec_b64 s[38:39], vcc
	s_cbranch_execz .Lcv1_491
	v_mad_u64_u32 v[72:73], s[8:9], v116, 24, v[114:115]
	v_lshl_add_u64 v[26:27], v[116:117], 2, v[72:73]
	global_load_dwordx4 v[30:33], v[72:73], off
	s_nop 0
	global_load_dwordx4 v[26:29], v[26:27], off

.Lcv1_492:
	s_or_b64 exec, exec, s[36:37]
	v_mov_b32_e32 v70, v0
	v_cmp_eq_f32_e32 vcc, 0, v119
	v_ashrrev_i32_e32 v72, 6, v70
	v_and_b32_e32 v73, 3, v70
	v_bitop3_b32 v111, v72, v70, 7 bitop3:0x78
	v_lshrrev_b32_e32 v72, 4, v70
	v_bfe_u32 v115, v70, 4, 3
	v_lshlrev_b32_e32 v116, 1, v73
	v_and_b32_e32 v114, 63, v70
	v_bitop3_b32 v73, v116, v72, 7 bitop3:0x78
	v_bitop3_b32 v72, v116, v115, 1 bitop3:0x36
	s_and_saveexec_b64 s[8:9], vcc
	s_xor_b64 s[36:37], exec, s[8:9]
	s_cbranch_execz .Lcv1_494
	v_lshlrev_b32_e32 v114, 9, v114
	v_lshlrev_b32_e32 v111, 4, v111
	v_add3_u32 v111, 0, v114, v111
	v_cvt_pk_bf16_f32 v114, v38, v42
	v_cvt_pk_bf16_f32 v115, v34, v46
	v_cvt_pk_bf16_f32 v116, v54, v58
	v_cvt_pk_bf16_f32 v117, v124, v66
	ds_write_b128 v111, v[114:117]
	v_cvt_pk_bf16_f32 v114, v39, v43
	v_cvt_pk_bf16_f32 v115, v35, v47
	v_cvt_pk_bf16_f32 v116, v55, v59
	v_cvt_pk_bf16_f32 v117, v125, v67
	ds_write_b128 v111, v[114:117] offset:128
	v_cvt_pk_bf16_f32 v115, v36, v48
	v_cvt_pk_bf16_f32 v34, v41, v45
	v_cvt_pk_bf16_f32 v35, v37, v49
	v_cvt_pk_bf16_f32 v36, v57, v61
	v_cvt_pk_bf16_f32 v37, v127, v69
	ds_write_b128 v111, v[34:37] offset:384
	v_lshlrev_b32_e32 v34, 5, v70
	v_and_b32_e32 v34, 0xffffff80, v34
	v_add_u32_e32 v42, 0, v34
	v_cvt_pk_bf16_f32 v114, v40, v44
	v_cvt_pk_bf16_f32 v116, v56, v60
	v_cvt_pk_bf16_f32 v117, v126, v68
	v_lshl_add_u32 v38, v73, 4, v42
	ds_write_b128 v111, v[114:117] offset:256
	s_waitcnt lgkmcnt(0)
	s_barrier
	ds_read_b128 v[34:37], v38
	v_lshl_add_u32 v54, v72, 4, v42
	ds_read_b128 v[42:45], v54
	ds_read_b128 v[38:41], v38 offset:16384
	v_mov_b32_e32 v111, v71
	s_waitcnt lgkmcnt(2)
	global_store_dwordx4 v[52:53], v[34:37], off
	ds_read_b128 v[34:37], v54 offset:16384
	s_waitcnt lgkmcnt(2)
	global_store_dwordx4 v[52:53], v[42:45], off offset:16
	s_nop 1
	v_lshlrev_b64 v[42:43], 8, v[110:111]
	v_lshl_add_u64 v[42:43], v[52:53], 0, v[42:43]
	s_waitcnt lgkmcnt(1)
	global_store_dwordx4 v[42:43], v[38:41], off
	s_waitcnt lgkmcnt(0)
	global_store_dwordx4 v[42:43], v[34:37], off offset:16
.Lcv1_494:
	s_andn2_saveexec_b64 s[36:37], s[36:37]
	s_cbranch_execz .Lcv1_413
	v_lshlrev_b32_e32 v116, 8, v114
	v_mul_f32_e32 v38, v38, v119
	v_mul_f32_e32 v42, v42, v119
	v_mov_b32_e32 v114, v71
	v_cvt_pk_fp8_f32 v114, v38, v42
	v_mul_f32_e32 v42, v54, v119
	v_mul_f32_e32 v38, v58, v119
	v_mov_b32_e32 v115, v71
	v_cvt_pk_fp8_f32 v115, v42, v38
	v_mul_f32_e32 v34, v34, v119
	v_mul_f32_e32 v46, v46, v119
	v_cvt_pk_fp8_f32 v114, v34, v46 op_sel:[0,0,1]
	v_mul_f32_e32 v34, v124, v119
	v_mul_f32_e32 v42, v66, v119
	v_cvt_pk_fp8_f32 v115, v34, v42 op_sel:[0,0,1]
	v_mul_f32_e32 v42, v39, v119
	v_mul_f32_e32 v43, v43, v119
	v_mov_b32_e32 v34, v71
	v_mul_f32_e32 v38, v35, v119
	v_cvt_pk_fp8_f32 v34, v42, v43
	v_mul_f32_e32 v42, v55, v119
	v_mul_f32_e32 v43, v59, v119
	v_mov_b32_e32 v35, v71
	v_cvt_pk_fp8_f32 v35, v42, v43
	v_mul_f32_e32 v42, v125, v119
	v_mul_f32_e32 v43, v67, v119
	v_mul_f32_e32 v39, v47, v119
	v_cvt_pk_fp8_f32 v35, v42, v43 op_sel:[0,0,1]
	v_mul_f32_e32 v43, v40, v119
	v_mul_f32_e32 v44, v44, v119
	v_mov_b32_e32 v42, v71
	v_cvt_pk_fp8_f32 v34, v38, v39 op_sel:[0,0,1]
	v_cvt_pk_fp8_f32 v42, v43, v44
	v_mul_f32_e32 v44, v56, v119
	v_mul_f32_e32 v39, v60, v119
	v_mov_b32_e32 v43, v71
	v_cvt_pk_fp8_f32 v43, v44, v39
	v_mul_f32_e32 v36, v36, v119
	v_mul_f32_e32 v38, v48, v119
	v_cvt_pk_fp8_f32 v42, v36, v38 op_sel:[0,0,1]
	v_mul_f32_e32 v36, v126, v119
	v_mul_f32_e32 v44, v68, v119
	v_cvt_pk_fp8_f32 v43, v36, v44 op_sel:[0,0,1]
	v_mul_f32_e32 v44, v41, v119
	v_mul_f32_e32 v45, v45, v119
	v_mov_b32_e32 v36, v71
	v_mul_f32_e32 v38, v37, v119
	v_cvt_pk_fp8_f32 v36, v44, v45
	v_mul_f32_e32 v44, v57, v119
	v_mul_f32_e32 v45, v61, v119
	v_mov_b32_e32 v37, v71
	v_cvt_pk_fp8_f32 v37, v44, v45
	v_mul_f32_e32 v39, v49, v119
	v_mul_f32_e32 v44, v127, v119
	v_mul_f32_e32 v45, v69, v119
	v_cvt_pk_fp8_f32 v36, v38, v39 op_sel:[0,0,1]
	v_cvt_pk_fp8_f32 v37, v44, v45 op_sel:[0,0,1]
	v_lshlrev_b32_e32 v44, 3, v111
	v_add3_u32 v44, 0, v116, v44
	ds_write2_b64 v44, v[114:115], v[34:35] offset1:8
	ds_write2_b64 v44, v[42:43], v[36:37] offset0:16 offset1:24
	v_lshlrev_b32_e32 v34, 4, v70
	v_and_b32_e32 v34, 0xffffffc0, v34
	v_add_u32_e32 v42, 0, v34
	v_lshl_add_u32 v34, v73, 3, v42
	s_waitcnt lgkmcnt(0)
	s_barrier
	ds_read2st64_b64 v[34:37], v34 offset1:16
	v_lshl_add_u32 v42, v72, 3, v42
	ds_read2st64_b64 v[42:45], v42 offset1:16
	v_mov_b32_e32 v111, v71
	s_waitcnt lgkmcnt(1)
	v_mov_b32_e32 v38, v34
	v_mov_b32_e32 v39, v35
	v_lshlrev_b64 v[34:35], 7, v[110:111]
	s_waitcnt lgkmcnt(0)
	v_mov_b32_e32 v40, v42
	v_mov_b32_e32 v41, v43
	v_mov_b32_e32 v42, v36
	v_mov_b32_e32 v43, v37
	v_lshl_add_u64 v[34:35], v[52:53], 0, v[34:35]
	global_store_dwordx4 v[52:53], v[38:41], off
	global_store_dwordx4 v[34:35], v[42:45], off

.Lcv2_418:
	s_or_b64 exec, exec, s[36:37]
	s_add_i32 s8, s2, -3
	s_and_b32 s8, s8, 3
	s_xor_b32 s8, s8, 2
	s_lshl_b32 s8, s8, 2
	s_add_i32 s8, s8, 0xa000
	v_mov_b32_e32 v72, s8
	ds_read_b32 v120, v72
	s_movk_i32 s8, 0x6b60
	s_waitcnt lgkmcnt(0)
	v_cmp_gt_i32_e32 vcc, s8, v120
	s_and_saveexec_b64 s[36:37], vcc
	s_cbranch_execz .Lcv2_417
	s_movk_i32 s8, 0x25f
	v_cmp_lt_i32_e32 vcc, s8, v120
	s_and_saveexec_b64 s[8:9], vcc
	s_xor_b64 s[38:39], exec, s[8:9]
	s_cbranch_execz .Lcv2_459
	s_movk_i32 s8, 0x35f
	v_cmp_lt_u32_e32 vcc, s8, v120
	s_and_saveexec_b64 s[8:9], vcc
	s_xor_b64 s[40:41], exec, s[8:9]
	s_cbranch_execz .Lcv2_453
	s_movk_i32 s8, 0x95f
	v_cmp_lt_u32_e32 vcc, s8, v120
	s_and_saveexec_b64 s[8:9], vcc
	s_xor_b64 s[42:43], exec, s[8:9]
	s_cbranch_execz .Lcv2_441
	s_movk_i32 s8, 0xb5f
	v_cmp_lt_u32_e32 vcc, s8, v120
	s_and_saveexec_b64 s[8:9], vcc
	s_xor_b64 s[44:45], exec, s[8:9]
	s_cbranch_execz .Lcv2_434
	s_movk_i32 s8, 0x4b5f
	v_cmp_lt_u32_e32 vcc, s8, v120
	s_and_saveexec_b64 s[8:9], vcc
	s_xor_b64 s[46:47], exec, s[8:9]
	s_cbranch_execz .Lcv2_428
	v_add_u32_e32 v72, 0xffffb4a0, v120
	v_lshrrev_b32_e32 v70, 6, v72
	v_lshlrev_b32_e32 v72, 5, v72
	v_and_b32_e32 v34, 0x700, v72
	v_lshlrev_b32_e32 v72, 6, v120
	v_and_b32_e32 v72, 0x1c0, v72
	v_mov_b32_e32 v73, v0
	s_andn2_b64 vcc, exec, s[24:25]
	s_cbranch_vccnz .Lcv2_426
	v_readlane_b32 s4, v254, 18
	v_lshlrev_b32_e32 v35, 2, v73
	v_lshlrev_b64 v[36:37], 22, v[70:71]
	v_readlane_b32 s16, v254, 30
	v_readlane_b32 s17, v254, 31
	v_and_or_b32 v35, v35, s33, v34
	v_ashrrev_i32_e32 v73, 3, v73
	v_lshl_add_u64 v[36:37], s[16:17], 0, v[36:37]
	v_lshlrev_b32_e32 v38, 2, v35
	v_mov_b32_e32 v39, v71
	v_and_b32_e32 v73, -8, v73
	v_lshl_add_u64 v[36:37], v[36:37], 0, v[38:39]
	v_add_u32_e32 v38, v73, v72
	v_ashrrev_i32_e32 v39, 31, v38
	v_lshlrev_b64 v[38:39], 13, v[38:39]
	v_lshl_add_u64 v[114:115], v[36:37], 0, v[38:39]
	v_readlane_b32 s5, v254, 19
	v_readlane_b32 s6, v254, 20
	v_readlane_b32 s7, v254, 21
	v_readlane_b32 s8, v254, 22
	v_readlane_b32 s9, v254, 23
	v_readlane_b32 s10, v254, 24
	v_readlane_b32 s11, v254, 25
	v_readlane_b32 s12, v254, 26
	v_readlane_b32 s13, v254, 27
	v_readlane_b32 s14, v254, 28
	v_readlane_b32 s15, v254, 29
	v_readlane_b32 s18, v254, 32
	v_readlane_b32 s19, v254, 33
	s_branch .Lcv2_427

.Lcv2_427:
	v_lshlrev_b64 v[36:37], 20, v[70:71]
	v_mov_b32_e32 v70, v0
	v_lshl_add_u64 v[36:37], s[74:75], 0, v[36:37]
	v_ashrrev_i32_e32 v35, 2, v70
	v_add_u32_e32 v34, v35, v34
	v_ashrrev_i32_e32 v35, 31, v34
	v_lshlrev_b64 v[34:35], 9, v[34:35]
	v_mov_b32_e32 v73, v71
	v_lshl_add_u64 v[34:35], v[36:37], 0, v[34:35]
	v_lshlrev_b32_e32 v70, 4, v70
	v_lshl_add_u64 v[72:73], v[34:35], 0, v[72:73]
	v_and_b32_e32 v70, 48, v70
	v_lshl_add_u64 v[106:107], v[72:73], 0, v[70:71]
.Lcv2_428:
	s_or_saveexec_b64 s[46:47], s[46:47]
	v_mov_b64_e32 v[116:117], 0x800
	v_mov_b32_e32 v108, 0x200
	v_mov_b32_e32 v109, 0x41800000
	s_xor_b64 exec, exec, s[46:47]
	s_cbranch_execz .Lcv2_437
	v_add_u32_e32 v40, 0xfffff4a0, v120
	v_mov_b32_e32 v41, v0
	v_lshlrev_b32_e32 v73, 2, v40
	v_lshlrev_b32_e32 v72, 2, v41
	v_lshrrev_b32_e32 v70, 7, v40
	v_and_b32_e32 v72, 0xfc, v72
	s_movk_i32 s8, 0x7f
	v_and_b32_e32 v73, 0x180, v73
	v_lshlrev_b64 v[34:35], 20, v[70:71]
	v_cmp_lt_u32_e32 vcc, s8, v72
	v_lshlrev_b32_e32 v36, 2, v73
	v_lshlrev_b32_e32 v72, 2, v72
	s_and_saveexec_b64 s[8:9], vcc
	s_xor_b64 s[64:65], exec, s[8:9]
	s_cbranch_execz .Lcv2_431
	v_readlane_b32 s4, v254, 18
	v_readlane_b32 s14, v254, 28
	v_readlane_b32 s15, v254, 29
	v_readlane_b32 s8, v254, 22
	v_readlane_b32 s9, v254, 23
	v_lshl_add_u64 v[34:35], v[34:35], 2, s[14:15]
	v_mov_b32_e32 v37, v71
	v_lshl_add_u64 v[34:35], v[34:35], 0, v[36:37]
	v_mov_b32_e32 v73, v71
	s_movk_i32 s8, 0xfe00
	v_lshl_add_u64 v[72:73], v[34:35], 0, v[72:73]
	s_mov_b32 s9, -1
	v_readlane_b32 s5, v254, 19
	v_readlane_b32 s6, v254, 20
	v_readlane_b32 s7, v254, 21
	v_readlane_b32 s10, v254, 24
	v_readlane_b32 s11, v254, 25
	v_readlane_b32 s12, v254, 26
	v_readlane_b32 s13, v254, 27
	v_readlane_b32 s16, v254, 30
	v_readlane_b32 s17, v254, 31
	v_readlane_b32 s18, v254, 32
	v_readlane_b32 s19, v254, 33
	v_lshl_add_u64 v[38:39], v[72:73], 0, s[8:9]
.Lcv2_431:
	s_andn2_saveexec_b64 s[64:65], s[64:65]
	s_cbranch_execz .Lcv2_433
	v_readlane_b32 s4, v254, 18
	v_readlane_b32 s12, v254, 26
	v_readlane_b32 s13, v254, 27
	v_mov_b32_e32 v37, v71
	v_mov_b32_e32 v73, v71
	v_lshl_add_u64 v[34:35], v[34:35], 2, s[12:13]
	v_lshl_add_u64 v[34:35], v[34:35], 0, v[36:37]
	v_lshl_add_u64 v[38:39], v[34:35], 0, v[72:73]
	v_readlane_b32 s5, v254, 19
	v_readlane_b32 s6, v254, 20
	v_readlane_b32 s7, v254, 21
	v_readlane_b32 s8, v254, 22
	v_readlane_b32 s9, v254, 23
	v_readlane_b32 s10, v254, 24
	v_readlane_b32 s11, v254, 25
	v_readlane_b32 s14, v254, 28
	v_readlane_b32 s15, v254, 29
	v_readlane_b32 s16, v254, 30
	v_readlane_b32 s17, v254, 31
	v_readlane_b32 s18, v254, 32
	v_readlane_b32 s19, v254, 33
.Lcv2_433:
	s_or_b64 exec, exec, s[64:65]
	v_lshlrev_b64 v[72:73], 21, v[70:71]
	v_lshlrev_b32_e32 v70, 3, v40
	v_and_b32_e32 v36, 0x300, v70
	v_lshlrev_b32_e32 v70, 6, v120
	v_ashrrev_i32_e32 v34, 3, v41
	v_and_b32_e32 v70, 0x7c0, v70
	v_and_b32_e32 v34, -8, v34
	v_add_u32_e32 v34, v34, v70
	v_ashrrev_i32_e32 v35, 31, v34
	v_lshlrev_b64 v[34:35], 11, v[34:35]
	v_lshl_add_u64 v[34:35], v[38:39], 0, v[34:35]
	v_cmp_ne_u64_e32 vcc, 0, v[38:39]
	v_mov_b32_e32 v37, v0
	v_lshl_add_u64 v[72:73], s[76:77], 0, v[72:73]
	v_cndmask_b32_e32 v114, 0, v34, vcc
	v_ashrrev_i32_e32 v34, 2, v37
	v_add_u32_e32 v34, v34, v36
	v_cndmask_b32_e32 v115, 0, v35, vcc
	v_ashrrev_i32_e32 v35, 31, v34
	v_lshlrev_b64 v[34:35], 11, v[34:35]
	v_lshl_add_u64 v[72:73], v[72:73], 0, v[34:35]
	v_lshl_add_u64 v[72:73], v[72:73], 0, v[70:71]
	v_lshlrev_b32_e32 v70, 4, v37
	v_and_b32_e32 v70, 48, v70
	v_lshl_add_u64 v[106:107], v[72:73], 0, v[70:71]
	v_mov_b64_e32 v[116:117], 0x200
	v_mov_b32_e32 v108, 0x800
	v_mov_b32_e32 v109, 0x42000000
	s_or_b64 exec, exec, s[46:47]

.Lcv2_435:
	v_add_u32_e32 v70, 0xfffff6a0, v120
	v_lshlrev_b32_e32 v72, 2, v70
	v_lshlrev_b32_e32 v70, 6, v70
	v_and_b32_e32 v72, 0x7fffff00, v72
	v_and_b32_e32 v70, 0xfc0, v70
	v_mov_b32_e32 v73, v0
	s_andn2_b64 vcc, exec, s[26:27]
	s_cbranch_vccnz .Lcv2_438
	v_lshlrev_b32_e32 v34, 2, v73
	v_ashrrev_i32_e32 v73, 3, v73
	v_and_b32_e32 v73, -8, v73
	v_readlane_b32 s4, v254, 18
	v_add_u32_e32 v36, v73, v70
	v_and_or_b32 v34, v34, s33, v72
	v_mov_b32_e32 v35, v71
	v_readlane_b32 s6, v254, 20
	v_readlane_b32 s7, v254, 21
	v_ashrrev_i32_e32 v37, 31, v36
	v_lshlrev_b64 v[36:37], 13, v[36:37]
	v_lshl_add_u64 v[34:35], v[34:35], 2, s[6:7]
	v_lshl_add_u64 v[114:115], v[34:35], 0, v[36:37]
	v_readlane_b32 s5, v254, 19
	v_readlane_b32 s8, v254, 22
	v_readlane_b32 s9, v254, 23
	v_readlane_b32 s10, v254, 24
	v_readlane_b32 s11, v254, 25
	v_readlane_b32 s12, v254, 26
	v_readlane_b32 s13, v254, 27
	v_readlane_b32 s14, v254, 28
	v_readlane_b32 s15, v254, 29
	v_readlane_b32 s16, v254, 30
	v_readlane_b32 s17, v254, 31
	v_readlane_b32 s18, v254, 32
	v_readlane_b32 s19, v254, 33
	s_branch .Lcv2_439

.Lcv2_439:
	v_mov_b32_e32 v34, v0
	v_mov_b64_e32 v[116:117], 0x800
	v_ashrrev_i32_e32 v73, 2, v34
	v_add_u32_e32 v72, v73, v72
	v_ashrrev_i32_e32 v73, 31, v72
	v_lshlrev_b64 v[72:73], 12, v[72:73]
	v_lshl_add_u64 v[72:73], s[78:79], 0, v[72:73]
	v_lshl_add_u64 v[72:73], v[72:73], 0, v[70:71]
	v_lshlrev_b32_e32 v70, 4, v34
	v_and_b32_e32 v70, 48, v70
	v_lshl_add_u64 v[106:107], v[72:73], 0, v[70:71]
	v_mov_b32_e32 v108, 0x1000
	v_mov_b32_e32 v109, 0x42800000

.Lcv2_441:
	s_andn2_saveexec_b64 s[42:43], s[42:43]
	s_cbranch_execz .Lcv2_452
	v_add_u32_e32 v70, 0xfffffca0, v120
	s_movk_i32 s8, 0x1ff
	v_cmp_lt_u32_e32 vcc, s8, v70
	v_lshlrev_b32_e32 v70, 3, v70
	v_and_b32_e32 v72, 0x7fffff00, v70
	s_and_saveexec_b64 s[8:9], vcc
	s_xor_b64 s[44:45], exec, s[8:9]
	s_cbranch_execz .Lcv2_446
	v_add_u32_e32 v72, 0xfffff000, v72
	v_lshlrev_b32_e32 v70, 6, v120
	s_movk_i32 s8, 0x2000
	v_and_b32_e32 v70, 0x7c0, v70
	v_mov_b32_e32 v73, v0
	v_cmp_gt_u32_e32 vcc, s8, v72
	v_mov_b64_e32 v[114:115], 0
	s_and_saveexec_b64 s[46:47], vcc
	v_lshlrev_b32_e32 v34, 2, v73
	v_ashrrev_i32_e32 v73, 3, v73
	v_and_or_b32 v34, v34, s33, v72
	v_mov_b32_e32 v35, v71
	v_and_b32_e32 v73, -8, v73
	v_lshl_add_u64 v[34:35], v[34:35], 2, s[28:29]
	v_add_u32_e32 v73, v73, v70
	v_mad_i64_i32 v[114:115], s[8:9], v73, s68, v[34:35]
	s_or_b64 exec, exec, s[46:47]
	v_mov_b32_e32 v34, v0
	s_nop 0
	v_ashrrev_i32_e32 v73, 2, v34
	v_add_u32_e32 v72, v73, v72
	v_ashrrev_i32_e32 v73, 31, v72
	v_lshlrev_b64 v[72:73], 11, v[72:73]
	v_lshl_add_u64 v[72:73], s[80:81], 0, v[72:73]
	v_lshl_add_u64 v[72:73], v[72:73], 0, v[70:71]
	v_lshlrev_b32_e32 v70, 4, v34
	v_and_b32_e32 v70, 48, v70
	v_lshl_add_u64 v[106:107], v[72:73], 0, v[70:71]
.Lcv2_446:
	s_andn2_saveexec_b64 s[44:45], s[44:45]
	s_cbranch_execz .Lcv2_451
	v_lshlrev_b32_e32 v70, 6, v120
	v_and_b32_e32 v70, 0x7c0, v70
	v_mov_b32_e32 v73, v0
	s_andn2_b64 vcc, exec, s[30:31]
	s_cbranch_vccnz .Lcv2_449
	v_lshlrev_b32_e32 v34, 2, v73
	v_ashrrev_i32_e32 v73, 3, v73
	v_and_or_b32 v34, v34, s33, v72
	v_mov_b32_e32 v35, v71
	v_and_b32_e32 v73, -8, v73
	v_lshl_add_u64 v[34:35], v[34:35], 2, s[62:63]
	v_add_u32_e32 v73, v73, v70
	v_mad_i64_i32 v[114:115], s[8:9], v73, s68, v[34:35]
	s_branch .Lcv2_450

.Lcv2_450:
	v_mov_b32_e32 v34, v0
	s_nop 0
	v_ashrrev_i32_e32 v73, 2, v34
	v_add_u32_e32 v72, v73, v72
	v_ashrrev_i32_e32 v73, 31, v72
	v_lshlrev_b64 v[72:73], 11, v[72:73]
	v_lshl_add_u64 v[72:73], s[82:83], 0, v[72:73]
	v_lshl_add_u64 v[72:73], v[72:73], 0, v[70:71]
	v_lshlrev_b32_e32 v70, 4, v34
	v_and_b32_e32 v70, 48, v70
	v_lshl_add_u64 v[106:107], v[72:73], 0, v[70:71]

.Lcv2_453:
	s_andn2_saveexec_b64 s[40:41], s[40:41]
	s_cbranch_execz .Lcv2_458
	v_lshl_add_u32 v70, v120, 3, v51
	v_and_b32_e32 v34, 0x7fffff00, v70
	v_lshlrev_b32_e32 v70, 6, v120
	v_and_b32_e32 v73, 0x7c0, v70
	v_mov_b32_e32 v72, v0
	s_andn2_b64 vcc, exec, s[34:35]
	s_cbranch_vccnz .Lcv2_456
	v_lshlrev_b32_e32 v70, 2, v72
	v_and_or_b32 v70, v70, s33, v34
	v_lshl_add_u64 v[36:37], v[70:71], 2, s[60:61]
	v_ashrrev_i32_e32 v70, 3, v72
	v_and_b32_e32 v70, -8, v70
	v_add_u32_e32 v38, v70, v73
	v_ashrrev_i32_e32 v39, 31, v38
	v_lshlrev_b64 v[38:39], 13, v[38:39]
	v_lshl_add_u64 v[114:115], v[36:37], 0, v[38:39]
	s_branch .Lcv2_457

.Lcv2_457:
	v_ashrrev_i32_e32 v70, 2, v72
	v_add_u32_e32 v34, v70, v34
	v_ashrrev_i32_e32 v35, 31, v34
	v_lshlrev_b64 v[34:35], 12, v[34:35]
	v_lshl_add_u64 v[34:35], s[84:85], 0, v[34:35]
	v_lshlrev_b32_e32 v70, 1, v73
	v_lshl_add_u64 v[34:35], v[34:35], 0, v[70:71]
	v_lshlrev_b32_e32 v70, 5, v72
	v_and_b32_e32 v70, 0x60, v70
	v_lshl_add_u64 v[106:107], v[34:35], 0, v[70:71]
	v_mov_b64_e32 v[116:117], 0x800
	v_mov_b32_e32 v108, 0x800
	v_mov_b32_e32 v109, 0

.Lcv2_459:
	s_andn2_saveexec_b64 s[38:39], s[38:39]
	s_cbranch_execz .Lcv2_483
	v_ashrrev_i32_e32 v70, 31, v120
	v_lshrrev_b32_e32 v70, 27, v70
	v_add_u32_e32 v70, v120, v70
	v_ashrrev_i32_e32 v37, 5, v70
	v_mov_b32_e32 v70, v0
	v_lshlrev_b32_e32 v36, 8, v37
	s_movk_i32 s8, 0x7ff
	v_lshlrev_b32_e32 v72, 2, v70
	v_and_or_b32 v72, v72, s33, v36
	v_cmp_lt_i32_e32 vcc, s8, v72
	s_mov_b64 s[42:43], -1
	s_and_saveexec_b64 s[40:41], vcc
	s_cbranch_execz .Lcv2_478
	s_movk_i32 s8, 0xbff
	v_cmp_lt_u32_e32 vcc, s8, v36
	s_mov_b64 s[44:45], 0
	s_and_saveexec_b64 s[8:9], vcc
	s_xor_b64 s[42:43], exec, s[8:9]
	s_cbranch_execz .Lcv2_475
	s_movk_i32 s8, 0x11ff
	v_cmp_lt_u32_e32 vcc, s8, v36
	s_mov_b64 s[46:47], 0
	s_and_saveexec_b64 s[8:9], vcc
	s_xor_b64 s[44:45], exec, s[8:9]
	s_cbranch_execz .Lcv2_472
	s_movk_i32 s8, 0x123f
	v_cmp_lt_u32_e32 vcc, s8, v72
	s_mov_b64 s[64:65], 0
	s_and_saveexec_b64 s[8:9], vcc
	s_xor_b64 s[46:47], exec, s[8:9]
	s_cbranch_execz .Lcv2_469
	s_movk_i32 s8, 0x1247
	v_cmp_lt_u32_e32 vcc, s8, v72
	s_and_saveexec_b64 s[8:9], vcc
	s_xor_b64 s[66:67], exec, s[8:9]
	s_movk_i32 s8, 0x1258
	v_cmp_gt_u32_e32 vcc, s8, v72
	s_and_b64 s[64:65], vcc, exec
	s_andn2_saveexec_b64 s[66:67], s[66:67]
	v_add_u32_e32 v72, 0xfffff600, v72
	s_or_b64 s[64:65], s[64:65], exec
	s_or_b64 exec, exec, s[66:67]
	s_and_b64 s[64:65], s[64:65], exec

.Lcv2_478:
	s_or_b64 exec, exec, s[40:41]
	v_mov_b64_e32 v[114:115], 0
	v_mov_b64_e32 v[34:35], 0
	s_and_saveexec_b64 s[40:41], s[42:43]
	s_cbranch_execz .Lcv2_480
	v_readlane_b32 s4, v254, 2
	v_ashrrev_i32_e32 v73, 31, v72
	v_readlane_b32 s12, v254, 10
	v_readlane_b32 s13, v254, 11
	v_readlane_b32 s5, v254, 3
	v_readlane_b32 s6, v254, 4
	v_lshl_add_u64 v[34:35], v[72:73], 2, s[12:13]
	v_readlane_b32 s7, v254, 5
	v_readlane_b32 s8, v254, 6
	v_readlane_b32 s9, v254, 7
	v_readlane_b32 s10, v254, 8
	v_readlane_b32 s11, v254, 9
	v_readlane_b32 s14, v254, 12
	v_readlane_b32 s15, v254, 13
	v_readlane_b32 s16, v254, 14
	v_readlane_b32 s17, v254, 15
	v_readlane_b32 s18, v254, 16
	v_readlane_b32 s19, v254, 17
.Lcv2_480:
	s_or_b64 exec, exec, s[40:41]
	v_lshlrev_b32_e32 v72, 5, v37
	v_sub_u32_e32 v72, v120, v72
	v_lshlrev_b32_e32 v72, 6, v72
	v_cmp_ne_u64_e32 vcc, 0, v[34:35]
	s_and_saveexec_b64 s[40:41], vcc
	v_ashrrev_i32_e32 v73, 3, v70
	v_and_b32_e32 v73, -8, v73
	v_add_u32_e32 v73, v73, v72
	s_movk_i32 s8, 0x4960
	v_mad_i64_i32 v[114:115], s[8:9], v73, s8, v[34:35]
	s_or_b64 exec, exec, s[40:41]
	v_ashrrev_i32_e32 v73, 2, v70
	v_add_u32_e32 v34, v73, v36
	v_ashrrev_i32_e32 v35, 31, v34
	v_lshlrev_b64 v[34:35], 12, v[34:35]
	v_lshl_add_u64 v[34:35], s[20:21], 0, v[34:35]
	v_ashrrev_i32_e32 v73, 31, v72
	v_lshlrev_b32_e32 v70, 5, v70
	v_lshl_add_u64 v[72:73], v[72:73], 1, v[34:35]
	v_and_b32_e32 v70, 0x60, v70
	v_lshl_add_u64 v[106:107], v[72:73], 0, v[70:71]
	v_mov_b64_e32 v[116:117], 0x1258
	v_mov_b32_e32 v108, 0x800
	v_mov_b32_e32 v109, 0
.Lcv2_483:
	s_or_b64 exec, exec, s[38:39]
	v_mov_b32_e32 v36, v71
	v_mov_b32_e32 v37, v71
	v_mov_b32_e32 v34, v71
	v_mov_b32_e32 v35, v71
	v_mov_b64_e32 v[40:41], v[36:37]
	v_mov_b64_e32 v[44:45], v[36:37]
	v_cmp_ne_u64_e32 vcc, 0, v[114:115]
	v_mov_b64_e32 v[38:39], v[34:35]
	v_mov_b64_e32 v[42:43], v[34:35]
	s_and_saveexec_b64 s[38:39], vcc
	s_cbranch_execz .Lcv2_485
	v_lshl_add_u64 v[72:73], v[116:117], 2, v[114:115]
	global_load_dwordx4 v[38:41], v[114:115], off
	global_load_dwordx4 v[42:45], v[72:73], off
.Lcv2_485:
	s_or_b64 exec, exec, s[38:39]
	v_mov_b64_e32 v[48:49], v[36:37]
	v_mov_b64_e32 v[46:47], v[34:35]
	s_and_saveexec_b64 s[38:39], vcc
	s_cbranch_execz .Lcv2_487
	v_lshl_add_u64 v[72:73], v[116:117], 3, v[114:115]
	v_lshl_add_u64 v[46:47], v[116:117], 2, v[72:73]
	global_load_dwordx4 v[34:37], v[72:73], off
	s_nop 0
	global_load_dwordx4 v[46:49], v[46:47], off
.Lcv2_487:
	s_or_b64 exec, exec, s[38:39]
	v_mov_b32_e32 v72, v71
	v_mov_b32_e32 v73, v71
	v_mov_b32_e32 v70, v71
	v_mov_b64_e32 v[56:57], v[72:73]
	v_mov_b64_e32 v[60:61], v[72:73]
	v_mov_b64_e32 v[54:55], v[70:71]
	v_mov_b64_e32 v[58:59], v[70:71]
	s_and_saveexec_b64 s[38:39], vcc
	s_cbranch_execz .Lcv2_489
	v_lshl_add_u64 v[72:73], v[116:117], 4, v[114:115]
	v_lshl_add_u64 v[58:59], v[116:117], 2, v[72:73]
	global_load_dwordx4 v[54:57], v[72:73], off
	s_nop 0
	global_load_dwordx4 v[58:61], v[58:59], off
.Lcv2_489:
	s_or_b64 exec, exec, s[38:39]
	v_mov_b32_e32 v127, 0
	v_mov_b32_e32 v126, 0
	v_mov_b32_e32 v125, 0
	v_mov_b32_e32 v124, 0
	v_mov_b32_e32 v69, 0
	v_mov_b32_e32 v68, 0
	v_mov_b32_e32 v67, 0
	v_mov_b32_e32 v66, 0
	s_and_saveexec_b64 s[38:39], vcc
	s_cbranch_execz .Lcv2_491
	v_mad_u64_u32 v[72:73], s[8:9], v116, 24, v[114:115]
	v_lshl_add_u64 v[66:67], v[116:117], 2, v[72:73]
	global_load_dwordx4 v[124:127], v[72:73], off
	s_nop 0
	global_load_dwordx4 v[66:69], v[66:67], off

.Lcv2_492:
	s_or_b64 exec, exec, s[36:37]
	v_mov_b32_e32 v70, v0
	v_cmp_eq_f32_e32 vcc, 0, v119
	v_ashrrev_i32_e32 v72, 6, v70
	v_and_b32_e32 v73, 3, v70
	v_bitop3_b32 v111, v72, v70, 7 bitop3:0x78
	v_lshrrev_b32_e32 v72, 4, v70
	v_bfe_u32 v115, v70, 4, 3
	v_lshlrev_b32_e32 v116, 1, v73
	v_and_b32_e32 v114, 63, v70
	v_bitop3_b32 v73, v116, v72, 7 bitop3:0x78
	v_bitop3_b32 v72, v116, v115, 1 bitop3:0x36
	s_and_saveexec_b64 s[8:9], vcc
	s_xor_b64 s[36:37], exec, s[8:9]
	s_cbranch_execz .Lcv2_494
	v_lshlrev_b32_e32 v114, 9, v114
	v_lshlrev_b32_e32 v111, 4, v111
	v_add3_u32 v111, 0, v114, v111
	v_cvt_pk_bf16_f32 v114, v78, v82
	v_cvt_pk_bf16_f32 v115, v74, v86
	v_cvt_pk_bf16_f32 v116, v90, v94
	v_cvt_pk_bf16_f32 v117, v98, v102
	ds_write_b128 v111, v[114:117]
	v_cvt_pk_bf16_f32 v114, v79, v83
	v_cvt_pk_bf16_f32 v115, v75, v87
	v_cvt_pk_bf16_f32 v116, v91, v95
	v_cvt_pk_bf16_f32 v117, v99, v103
	ds_write_b128 v111, v[114:117] offset:128
	v_cvt_pk_bf16_f32 v115, v76, v88
	v_cvt_pk_bf16_f32 v74, v81, v85
	v_cvt_pk_bf16_f32 v75, v77, v89
	v_cvt_pk_bf16_f32 v76, v93, v97
	v_cvt_pk_bf16_f32 v77, v101, v105
	ds_write_b128 v111, v[74:77] offset:384
	v_lshlrev_b32_e32 v74, 5, v70
	v_and_b32_e32 v74, 0xffffff80, v74
	v_add_u32_e32 v82, 0, v74
	v_cvt_pk_bf16_f32 v114, v80, v84
	v_cvt_pk_bf16_f32 v116, v92, v96
	v_cvt_pk_bf16_f32 v117, v100, v104
	v_lshl_add_u32 v78, v73, 4, v82
	ds_write_b128 v111, v[114:117] offset:256
	s_waitcnt lgkmcnt(0)
	s_barrier
	ds_read_b128 v[74:77], v78
	v_lshl_add_u32 v90, v72, 4, v82
	ds_read_b128 v[82:85], v90
	ds_read_b128 v[78:81], v78 offset:16384
	v_mov_b32_e32 v111, v71
	s_waitcnt lgkmcnt(2)
	global_store_dwordx4 v[52:53], v[74:77], off
	ds_read_b128 v[74:77], v90 offset:16384
	s_waitcnt lgkmcnt(2)
	global_store_dwordx4 v[52:53], v[82:85], off offset:16
	s_nop 1
	v_lshlrev_b64 v[82:83], 8, v[110:111]
	v_lshl_add_u64 v[82:83], v[52:53], 0, v[82:83]
	s_waitcnt lgkmcnt(1)
	global_store_dwordx4 v[82:83], v[78:81], off
	s_waitcnt lgkmcnt(0)
	global_store_dwordx4 v[82:83], v[74:77], off offset:16
.Lcv2_494:
	s_andn2_saveexec_b64 s[36:37], s[36:37]
	s_cbranch_execz .Lcv2_413
	v_lshlrev_b32_e32 v116, 8, v114
	v_mul_f32_e32 v78, v78, v119
	v_mul_f32_e32 v82, v82, v119
	v_mov_b32_e32 v114, v71
	v_cvt_pk_fp8_f32 v114, v78, v82
	v_mul_f32_e32 v82, v90, v119
	v_mul_f32_e32 v78, v94, v119
	v_mov_b32_e32 v115, v71
	v_cvt_pk_fp8_f32 v115, v82, v78
	v_mul_f32_e32 v74, v74, v119
	v_mul_f32_e32 v86, v86, v119
	v_cvt_pk_fp8_f32 v114, v74, v86 op_sel:[0,0,1]
	v_mul_f32_e32 v74, v98, v119
	v_mul_f32_e32 v82, v102, v119
	v_cvt_pk_fp8_f32 v115, v74, v82 op_sel:[0,0,1]
	v_mul_f32_e32 v82, v79, v119
	v_mul_f32_e32 v83, v83, v119
	v_mov_b32_e32 v74, v71
	v_mul_f32_e32 v78, v75, v119
	v_cvt_pk_fp8_f32 v74, v82, v83
	v_mul_f32_e32 v82, v91, v119
	v_mul_f32_e32 v83, v95, v119
	v_mov_b32_e32 v75, v71
	v_cvt_pk_fp8_f32 v75, v82, v83
	v_mul_f32_e32 v82, v99, v119
	v_mul_f32_e32 v83, v103, v119
	v_mul_f32_e32 v79, v87, v119
	v_cvt_pk_fp8_f32 v75, v82, v83 op_sel:[0,0,1]
	v_mul_f32_e32 v83, v80, v119
	v_mul_f32_e32 v84, v84, v119
	v_mov_b32_e32 v82, v71
	v_cvt_pk_fp8_f32 v74, v78, v79 op_sel:[0,0,1]
	v_cvt_pk_fp8_f32 v82, v83, v84
	v_mul_f32_e32 v84, v92, v119
	v_mul_f32_e32 v79, v96, v119
	v_mov_b32_e32 v83, v71
	v_cvt_pk_fp8_f32 v83, v84, v79
	v_mul_f32_e32 v76, v76, v119
	v_mul_f32_e32 v78, v88, v119
	v_cvt_pk_fp8_f32 v82, v76, v78 op_sel:[0,0,1]
	v_mul_f32_e32 v76, v100, v119
	v_mul_f32_e32 v84, v104, v119
	v_cvt_pk_fp8_f32 v83, v76, v84 op_sel:[0,0,1]
	v_mul_f32_e32 v84, v81, v119
	v_mul_f32_e32 v85, v85, v119
	v_mov_b32_e32 v76, v71
	v_mul_f32_e32 v78, v77, v119
	v_cvt_pk_fp8_f32 v76, v84, v85
	v_mul_f32_e32 v84, v93, v119
	v_mul_f32_e32 v85, v97, v119
	v_mov_b32_e32 v77, v71
	v_cvt_pk_fp8_f32 v77, v84, v85
	v_mul_f32_e32 v79, v89, v119
	v_mul_f32_e32 v84, v101, v119
	v_mul_f32_e32 v85, v105, v119
	v_cvt_pk_fp8_f32 v76, v78, v79 op_sel:[0,0,1]
	v_cvt_pk_fp8_f32 v77, v84, v85 op_sel:[0,0,1]
	v_lshlrev_b32_e32 v84, 3, v111
	v_add3_u32 v84, 0, v116, v84
	ds_write2_b64 v84, v[114:115], v[74:75] offset1:8
	ds_write2_b64 v84, v[82:83], v[76:77] offset0:16 offset1:24
	v_lshlrev_b32_e32 v74, 4, v70
	v_and_b32_e32 v74, 0xffffffc0, v74
	v_add_u32_e32 v82, 0, v74
	v_lshl_add_u32 v74, v73, 3, v82
	s_waitcnt lgkmcnt(0)
	s_barrier
	ds_read2st64_b64 v[74:77], v74 offset1:16
	v_lshl_add_u32 v82, v72, 3, v82
	ds_read2st64_b64 v[82:85], v82 offset1:16
	v_mov_b32_e32 v111, v71
	s_waitcnt lgkmcnt(1)
	v_mov_b32_e32 v78, v74
	v_mov_b32_e32 v79, v75
	v_lshlrev_b64 v[74:75], 7, v[110:111]
	s_waitcnt lgkmcnt(0)
	v_mov_b32_e32 v80, v82
	v_mov_b32_e32 v81, v83
	v_mov_b32_e32 v82, v76
	v_mov_b32_e32 v83, v77
	v_lshl_add_u64 v[74:75], v[52:53], 0, v[74:75]
	global_store_dwordx4 v[52:53], v[78:81], off
	global_store_dwordx4 v[74:75], v[82:85], off
.Lcv2_413:
	s_or_b64 exec, exec, s[36:37]
	s_movk_i32 s8, 0x6b5f
	v_cmp_lt_i32_e32 vcc, s8, v1
	s_add_i32 s2, s2, 1
	s_or_b64 s[22:23], vcc, s[22:23]
	v_mov_b32_e32 v1, v120
	v_mov_b64_e32 v[72:73], v[106:107]
	v_mov_b32_e32 v114, v108
	v_mov_b32_e32 v111, v109
	v_mov_b64_e32 v[52:53], v[112:113]
	v_mov_b32_e32 v110, v118
	v_mov_b32_e32 v119, v65
	s_barrier
	s_andn2_b64 exec, exec, s[22:23]
	s_cbranch_execz .LBB0_496
	s_branch .Lcv0_414

.LBB0_497:
	s_cmp_lg_u32 s100, 1
	s_cbranch_scc1 .Lcq_ret_done
	s_mov_b32 s100, 2
	s_mov_b64 s[0:1], -1
	s_branch .LBB0_1177

.LBB0_1177:
	s_bitcmp0_b32 s93, 0
	s_cbranch_scc1 .Lp4_go
	s_cmp_lg_u32 s100, 0
	s_cbranch_scc1 .Lp4_go
	s_mov_b32 s100, 1
	v_readlane_b32 s6, v254, 0
	v_readlane_b32 s7, v254, 1
	s_sub_u32 s6, s6, 0xd0
	s_subb_u32 s7, s7, 0
	s_load_dwordx16 s[48:63], s[6:7], 0x40
	s_waitcnt lgkmcnt(0)
	s_mov_b64 s[2:3], exec
	s_branch .LBB0_251
